# v39 + comb phase keeps two tokens of operands in flight (loop unrolled by two on two register sets, counted waits)
# baseline (speedup 1.0000x reference)
.LBB0_2051:
	v_readlane_b32 s0, v253, 60
	v_readlane_b32 s1, v253, 61
	s_waitcnt lgkmcnt(0)
	s_barrier
	v_mbcnt_lo_u32_b32 v4, -1, 0
	v_mbcnt_hi_u32_b32 v4, -1, v4
	s_and_b64 vcc, exec, s[0:1]
	s_cbranch_vccz .LBB0_2056
	s_lshl_b64 s[4:5], s[38:39], 16
	v_readlane_b32 s0, v254, 8
	s_add_u32 s2, s0, s4
	v_readlane_b32 s0, v254, 9
	s_addc_u32 s3, s0, s5
	v_readlane_b32 s0, v254, 14
	s_add_u32 s12, s0, s4
	v_readlane_b32 s0, v254, 15
	s_addc_u32 s13, s0, s5
	v_ashrrev_i32_e32 v5, 31, v4
	v_readlane_b32 s0, v254, 18
	v_lshlrev_b64 v[2:3], 2, v[4:5]
	v_readlane_b32 s1, v254, 19
	v_lshlrev_b32_e32 v0, 5, v4
	v_and_b32_e32 v0, 0x60, v0
	v_lshl_add_u64 v[8:9], s[0:1], 0, v[2:3]
	s_mov_b32 s0, 0x400000
	v_add_co_u32_e32 v10, vcc, s0, v8
	s_mov_b32 s0, 0x800000
	s_nop 0
	v_addc_co_u32_e32 v11, vcc, 0, v9, vcc
	global_load_dword v12, v[8:9], off
	global_load_dword v14, v[10:11], off
	v_add_co_u32_e32 v10, vcc, s0, v8
	s_mov_b32 s0, 0xc00000
	s_nop 0
	v_addc_co_u32_e32 v11, vcc, 0, v9, vcc
	global_load_dword v13, v[10:11], off
	v_add_co_u32_e32 v10, vcc, s0, v8
	s_mov_b32 s0, 0x1000000
	s_nop 0
	v_addc_co_u32_e32 v11, vcc, 0, v9, vcc
	global_load_dword v15, v[10:11], off
	v_add_co_u32_e32 v10, vcc, s0, v8
	s_mov_b32 s0, 0x1400000
	s_nop 0
	v_addc_co_u32_e32 v11, vcc, 0, v9, vcc
	global_load_dword v16, v[10:11], off
	v_add_co_u32_e32 v10, vcc, s0, v8
	s_mov_b32 s0, 0x1800000
	s_nop 0
	v_addc_co_u32_e32 v11, vcc, 0, v9, vcc
	global_load_dword v17, v[10:11], off
	v_add_co_u32_e32 v10, vcc, s0, v8
	s_mov_b32 s0, 0x1c00000
	s_nop 0
	v_addc_co_u32_e32 v11, vcc, 0, v9, vcc
	global_load_dword v18, v[10:11], off
	v_add_co_u32_e32 v10, vcc, s0, v8
	s_brev_b32 s0, 64
	s_nop 0
	v_addc_co_u32_e32 v11, vcc, 0, v9, vcc
	global_load_dword v19, v[10:11], off
	v_add_co_u32_e32 v10, vcc, s0, v8
	s_mov_b32 s0, 0x2400000
	s_nop 0
	v_addc_co_u32_e32 v11, vcc, 0, v9, vcc
	global_load_dword v20, v[10:11], off
	v_add_co_u32_e32 v10, vcc, s0, v8
	s_mov_b32 s0, 0x2800000
	s_nop 0
	v_addc_co_u32_e32 v11, vcc, 0, v9, vcc
	global_load_dword v21, v[10:11], off
	v_add_co_u32_e32 v10, vcc, s0, v8
	s_mov_b32 s0, 0x2c00000
	s_nop 0
	v_addc_co_u32_e32 v11, vcc, 0, v9, vcc
	global_load_dword v22, v[10:11], off
	v_add_co_u32_e32 v10, vcc, s0, v8
	s_mov_b32 s0, 0x3000000
	s_nop 0
	v_addc_co_u32_e32 v11, vcc, 0, v9, vcc
	global_load_dword v24, v[10:11], off
	v_add_co_u32_e32 v10, vcc, s0, v8
	s_mov_b32 s0, 0x3400000
	s_nop 0
	v_addc_co_u32_e32 v11, vcc, 0, v9, vcc
	global_load_dword v25, v[10:11], off
	v_add_co_u32_e32 v10, vcc, s0, v8
	s_mov_b32 s0, 0x3800000
	s_nop 0
	v_addc_co_u32_e32 v11, vcc, 0, v9, vcc
	global_load_dword v26, v[10:11], off
	v_add_co_u32_e32 v10, vcc, s0, v8
	v_ashrrev_i32_e32 v1, 2, v4
	s_nop 0
	v_addc_co_u32_e32 v11, vcc, 0, v9, vcc
	s_mov_b32 s0, 0x3c00000
	v_add_u32_e32 v6, v0, v1
	v_add_co_u32_e32 v8, vcc, s0, v8
	v_ashrrev_i32_e32 v7, 31, v6
	s_nop 0
	v_addc_co_u32_e32 v9, vcc, 0, v9, vcc
	v_readlane_b32 s0, v254, 20
	v_lshlrev_b32_e32 v0, 1, v4
	global_load_dword v27, v[10:11], off
	global_load_dword v28, v[8:9], off
	v_lshlrev_b64 v[8:9], 2, v[6:7]
	v_readlane_b32 s1, v254, 21
	v_ashrrev_i32_e32 v1, 31, v0
	v_lshlrev_b64 v[32:33], 2, v[0:1]
	v_lshl_add_u64 v[10:11], s[0:1], 0, v[8:9]
	v_readlane_b32 s0, v254, 24
	v_readlane_b32 s1, v254, 25
	global_load_dword v30, v[10:11], off
	global_load_dword v29, v[10:11], off offset:64
	v_lshl_add_u64 v[0:1], s[0:1], 0, v[32:33]
	global_load_dwordx2 v[10:11], v[0:1], off
	v_readlane_b32 s0, v255, 35
	v_readlane_b32 s1, v255, 36
	v_readlane_b32 s14, v255, 28
	v_cmp_eq_u32_e64 s[4:5], 0, v4
	v_lshl_add_u64 v[0:1], s[0:1], 0, v[2:3]
	v_readlane_b32 s0, v254, 22
	v_readlane_b32 s1, v254, 23
	v_lshl_add_u64 v[4:5], s[82:83], 0, v[8:9]
	v_readlane_b32 s15, v255, 29
	v_lshl_add_u64 v[2:3], s[0:1], 0, v[32:33]
	v_readlane_b32 s0, v255, 30
	v_readlane_b32 s1, v255, 31
	s_mov_b32 s18, s80
	s_nop 0
	v_lshl_add_u64 v[6:7], s[0:1], 0, v[6:7]
	v_readlane_b32 s0, v255, 20
	s_nop 1
	s_add_i32 s26, s80, s0
	s_cmpk_lt_i32 s26, 0x4000
	s_cselect_b32 s26, s26, s80
	s_ashr_i32 s27, s26, 31
	s_lshl_b64 s[28:29], s[26:27], 8
	s_lshl_b64 s[26:27], s[26:27], 9
	v_lshl_add_u64 v[164:165], v[0:1], 0, s[28:29]
	global_load_dword v112, v[164:165], off
	s_mov_b32 s31, 0x400000
	v_add_co_u32_e32 v166, vcc, s31, v164
	s_nop 1
	v_addc_co_u32_e32 v167, vcc, 0, v165, vcc
	global_load_dword v114, v[166:167], off
	s_mov_b32 s31, 0x800000
	v_add_co_u32_e32 v166, vcc, s31, v164
	s_nop 1
	v_addc_co_u32_e32 v167, vcc, 0, v165, vcc
	global_load_dword v113, v[166:167], off
	s_mov_b32 s31, 0xc00000
	v_add_co_u32_e32 v166, vcc, s31, v164
	s_nop 1
	v_addc_co_u32_e32 v167, vcc, 0, v165, vcc
	global_load_dword v115, v[166:167], off
	s_mov_b32 s31, 0x1000000
	v_add_co_u32_e32 v166, vcc, s31, v164
	s_nop 1
	v_addc_co_u32_e32 v167, vcc, 0, v165, vcc
	global_load_dword v116, v[166:167], off
	s_mov_b32 s31, 0x1400000
	v_add_co_u32_e32 v166, vcc, s31, v164
	s_nop 1
	v_addc_co_u32_e32 v167, vcc, 0, v165, vcc
	global_load_dword v117, v[166:167], off
	s_mov_b32 s31, 0x1800000
	v_add_co_u32_e32 v166, vcc, s31, v164
	s_nop 1
	v_addc_co_u32_e32 v167, vcc, 0, v165, vcc
	global_load_dword v118, v[166:167], off
	s_mov_b32 s31, 0x1c00000
	v_add_co_u32_e32 v166, vcc, s31, v164
	s_nop 1
	v_addc_co_u32_e32 v167, vcc, 0, v165, vcc
	global_load_dword v119, v[166:167], off
	s_mov_b32 s31, 0x2000000
	v_add_co_u32_e32 v166, vcc, s31, v164
	s_nop 1
	v_addc_co_u32_e32 v167, vcc, 0, v165, vcc
	global_load_dword v120, v[166:167], off
	s_mov_b32 s31, 0x2400000
	v_add_co_u32_e32 v166, vcc, s31, v164
	s_nop 1
	v_addc_co_u32_e32 v167, vcc, 0, v165, vcc
	global_load_dword v121, v[166:167], off
	s_mov_b32 s31, 0x2800000
	v_add_co_u32_e32 v166, vcc, s31, v164
	s_nop 1
	v_addc_co_u32_e32 v167, vcc, 0, v165, vcc
	global_load_dword v122, v[166:167], off
	s_mov_b32 s31, 0x2c00000
	v_add_co_u32_e32 v166, vcc, s31, v164
	s_nop 1
	v_addc_co_u32_e32 v167, vcc, 0, v165, vcc
	global_load_dword v124, v[166:167], off
	s_mov_b32 s31, 0x3000000
	v_add_co_u32_e32 v166, vcc, s31, v164
	s_nop 1
	v_addc_co_u32_e32 v167, vcc, 0, v165, vcc
	global_load_dword v125, v[166:167], off
	s_mov_b32 s31, 0x3400000
	v_add_co_u32_e32 v166, vcc, s31, v164
	s_nop 1
	v_addc_co_u32_e32 v167, vcc, 0, v165, vcc
	global_load_dword v126, v[166:167], off
	s_mov_b32 s31, 0x3800000
	v_add_co_u32_e32 v166, vcc, s31, v164
	s_nop 1
	v_addc_co_u32_e32 v167, vcc, 0, v165, vcc
	global_load_dword v127, v[166:167], off
	s_mov_b32 s31, 0x3c00000
	v_add_co_u32_e32 v166, vcc, s31, v164
	s_nop 1
	v_addc_co_u32_e32 v167, vcc, 0, v165, vcc
	global_load_dword v128, v[166:167], off
	v_lshl_add_u64 v[166:167], v[4:5], 0, s[26:27]
	global_load_dword v130, v[166:167], off
	global_load_dword v129, v[166:167], off offset:64
	v_lshl_add_u64 v[166:167], v[2:3], 0, s[26:27]
	global_load_dwordx2 v[110:111], v[166:167], off
	s_waitcnt vmcnt(19)
.LBB0_2054:
	v_mov_b64_e32 v[8:9], v[10:11]
	v_lshrrev_b32_e32 v10, 5, v30
	v_and_b32_e32 v10, 0x7fffffc, v10
	global_load_dword v33, v10, s[2:3]
	v_lshrrev_b32_e32 v11, 5, v29
	v_and_b32_e32 v11, 0x7fffffc, v11
	global_load_dword v34, v11, s[2:3]
	global_load_dword v35, v10, s[12:13]
	global_load_dword v23, v11, s[12:13]
	v_readlane_b32 s0, v255, 20
	s_mov_b32 s6, s18
	s_add_i32 s18, s18, s0
	s_cmpk_gt_i32 s18, 0x3fff
	s_cselect_b64 s[16:17], -1, 0
	s_add_i32 s22, s18, s0
	s_cmpk_lt_i32 s22, 0x4000
	s_cselect_b32 s6, s22, s6
	s_ashr_i32 s7, s6, 31
	s_lshl_b64 s[20:21], s[6:7], 8
	v_lshl_add_u64 v[10:11], v[0:1], 0, s[20:21]
	s_mov_b32 s0, 0x400000
	v_mov_b32_e32 v31, v14
	v_add_co_u32_e32 v14, vcc, s0, v10
	v_bfe_i32 v37, v15, 0, 16
	v_ashrrev_i32_e32 v38, 16, v15
	v_addc_co_u32_e32 v15, vcc, 0, v11, vcc
	s_mov_b32 s0, 0x800000
	v_bfe_i32 v39, v16, 0, 16
	v_ashrrev_i32_e32 v40, 16, v16
	v_add_co_u32_e32 v16, vcc, s0, v10
	v_bfe_i32 v41, v17, 0, 16
	v_ashrrev_i32_e32 v42, 16, v17
	v_addc_co_u32_e32 v17, vcc, 0, v11, vcc
	s_mov_b32 s0, 0xc00000
	v_mov_b32_e32 v32, v12
	v_bfe_i32 v30, v13, 0, 16
	v_ashrrev_i32_e32 v36, 16, v13
	global_load_dword v12, v[10:11], off
	global_load_dword v13, v[16:17], off
	v_add_co_u32_e32 v16, vcc, s0, v10
	global_load_dword v14, v[14:15], off
	s_nop 0
	v_addc_co_u32_e32 v17, vcc, 0, v11, vcc
	s_mov_b32 s0, 0x1000000
	global_load_dword v15, v[16:17], off
	v_add_co_u32_e32 v16, vcc, s0, v10
	s_mov_b32 s0, 0x1400000
	s_nop 0
	v_addc_co_u32_e32 v17, vcc, 0, v11, vcc
	v_bfe_i32 v43, v18, 0, 16
	v_ashrrev_i32_e32 v44, 16, v18
	v_add_co_u32_e32 v18, vcc, s0, v10
	v_bfe_i32 v45, v19, 0, 16
	v_ashrrev_i32_e32 v46, 16, v19
	v_addc_co_u32_e32 v19, vcc, 0, v11, vcc
	s_mov_b32 s0, 0x1800000
	global_load_dword v16, v[16:17], off
	v_bfe_i32 v47, v20, 0, 16
	global_load_dword v17, v[18:19], off
	v_add_co_u32_e32 v18, vcc, s0, v10
	s_mov_b32 s0, 0x1c00000
	s_nop 0
	v_addc_co_u32_e32 v19, vcc, 0, v11, vcc
	v_ashrrev_i32_e32 v48, 16, v20
	v_add_co_u32_e32 v20, vcc, s0, v10
	v_bfe_i32 v49, v21, 0, 16
	v_ashrrev_i32_e32 v50, 16, v21
	v_addc_co_u32_e32 v21, vcc, 0, v11, vcc
	s_brev_b32 s0, 64
	global_load_dword v18, v[18:19], off
	v_bfe_i32 v53, v24, 0, 16
	global_load_dword v19, v[20:21], off
	v_add_co_u32_e32 v20, vcc, s0, v10
	s_mov_b32 s0, 0x2400000
	s_nop 0
	v_addc_co_u32_e32 v21, vcc, 0, v11, vcc
	v_ashrrev_i32_e32 v54, 16, v24
	v_add_co_u32_e32 v24, vcc, s0, v10
	v_bfe_i32 v55, v25, 0, 16
	v_ashrrev_i32_e32 v56, 16, v25
	v_addc_co_u32_e32 v25, vcc, 0, v11, vcc
	s_mov_b32 s0, 0x2800000
	global_load_dword v20, v[20:21], off
	v_bfe_i32 v51, v22, 0, 16
	global_load_dword v21, v[24:25], off
	v_add_co_u32_e32 v24, vcc, s0, v10
	s_mov_b32 s0, 0x2c00000
	s_nop 0
	v_addc_co_u32_e32 v25, vcc, 0, v11, vcc
	v_ashrrev_i32_e32 v52, 16, v22
	global_load_dword v22, v[24:25], off
	v_add_co_u32_e32 v24, vcc, s0, v10
	s_mov_b32 s0, 0x3000000
	s_nop 0
	v_addc_co_u32_e32 v25, vcc, 0, v11, vcc
	v_bfe_i32 v57, v26, 0, 16
	v_ashrrev_i32_e32 v58, 16, v26
	v_add_co_u32_e32 v26, vcc, s0, v10
	v_bfe_i32 v59, v27, 0, 16
	v_ashrrev_i32_e32 v60, 16, v27
	v_addc_co_u32_e32 v27, vcc, 0, v11, vcc
	s_mov_b32 s0, 0x3400000
	global_load_dword v24, v[24:25], off
	v_bfe_i32 v61, v28, 0, 16
	global_load_dword v25, v[26:27], off
	v_add_co_u32_e32 v26, vcc, s0, v10
	s_mov_b32 s0, 0x3800000
	s_nop 0
	v_addc_co_u32_e32 v27, vcc, 0, v11, vcc
	v_ashrrev_i32_e32 v62, 16, v28
	v_add_co_u32_e32 v28, vcc, s0, v10
	s_mov_b32 s0, 0x3c00000
	s_nop 0
	v_addc_co_u32_e32 v29, vcc, 0, v11, vcc
	v_add_co_u32_e32 v10, vcc, s0, v10
	global_load_dword v26, v[26:27], off
	s_nop 0
	v_addc_co_u32_e32 v11, vcc, 0, v11, vcc
	global_load_dword v27, v[28:29], off
	s_lshl_b64 s[6:7], s[6:7], 9
	global_load_dword v28, v[10:11], off
	v_add_u32_sdwa v10, sext(v31), sext(v32) dst_sel:DWORD dst_unused:UNUSED_PAD src0_sel:WORD_0 src1_sel:WORD_0
	v_add3_u32 v10, v10, v30, v37
	v_add3_u32 v10, v10, v39, v41
	v_add3_u32 v10, v10, v43, v45
	v_add3_u32 v10, v10, v47, v49
	v_add_u32_sdwa v11, sext(v31), sext(v32) dst_sel:DWORD dst_unused:UNUSED_PAD src0_sel:WORD_1 src1_sel:WORD_1
	v_add3_u32 v10, v10, v51, v53
	v_add3_u32 v11, v11, v36, v38
	v_add3_u32 v10, v10, v55, v57
	v_add3_u32 v11, v11, v40, v42
	v_add3_u32 v31, v10, v59, v61
	v_add3_u32 v11, v11, v44, v46
	v_cvt_f32_i32_e32 v31, v31
	v_add3_u32 v11, v11, v48, v50
	v_add3_u32 v11, v11, v52, v54
	v_add3_u32 v11, v11, v56, v58
	s_waitcnt vmcnt(19)
	v_mul_f32_e32 v33, 0x40810204, v33
	v_add3_u32 v32, v11, v60, v62
	v_lshl_add_u64 v[10:11], v[4:5], 0, s[6:7]
	v_mul_f32_e32 v31, v33, v31
	global_load_dword v30, v[10:11], off
	global_load_dword v29, v[10:11], off offset:64
	v_lshl_add_u64 v[10:11], v[2:3], 0, s[6:7]
	v_mul_f32_e32 v33, 0x3d372713, v31
	global_load_dwordx2 v[10:11], v[10:11], off
	v_mul_f32_e32 v33, v31, v33
	v_fma_f32 v33, v31, v33, v31
	v_mul_f32_e32 v33, 0x3f4c422a, v33
	v_add_f32_e32 v33, v33, v33
	v_mul_f32_e32 v33, 0xbfb8aa3b, v33
	v_exp_f32_e32 v33, v33
	s_waitcnt vmcnt(21)
	v_mul_f32_e32 v34, 0x40810204, v34
	s_mov_b32 s0, 0x42fe0000
	v_readlane_b32 s1, v255, 21
	v_add_f32_e32 v33, 1.0, v33
	v_rcp_f32_e32 v33, v33
	s_nop 0
	v_mul_f32_e32 v31, v31, v33
	v_mul_f32_e32 v8, v8, v31
	s_waitcnt vmcnt(20)
	v_mul_f32_e32 v31, v35, v8
	v_cvt_f32_i32_e32 v8, v32
	v_mul_f32_e32 v8, v34, v8
	v_mul_f32_e32 v32, 0x3d372713, v8
	v_mul_f32_e32 v32, v8, v32
	v_fma_f32 v32, v8, v32, v8
	v_mul_f32_e32 v32, 0x3f4c422a, v32
	v_add_f32_e32 v32, v32, v32
	v_mul_f32_e32 v32, 0xbfb8aa3b, v32
	v_exp_f32_e32 v32, v32
	s_nop 0
	v_add_f32_e32 v32, 1.0, v32
	v_rcp_f32_e32 v32, v32
	s_nop 0
	v_mul_f32_e32 v8, v8, v32
	v_mul_f32_e32 v8, v9, v8
	s_waitcnt vmcnt(19)
	v_mul_f32_e32 v9, v23, v8
	v_max_f32_e64 v8, |v31|, |v9|
	v_mov_b32_e32 v23, v201
	s_nop 1
	v_mov_b32_dpp v23, v8 row_ror:1 row_mask:0xf bank_mask:0xf
	v_max_f32_e32 v23, v23, v23
	v_max_f32_e32 v8, v8, v23
	v_mov_b32_e32 v23, v201
	s_nop 1
	v_mov_b32_dpp v23, v8 row_ror:2 row_mask:0xf bank_mask:0xf
	v_max_f32_e32 v23, v23, v23
	v_max_f32_e32 v8, v8, v23
	v_mov_b32_e32 v23, v201
	s_nop 1
	v_mov_b32_dpp v23, v8 row_ror:4 row_mask:0xf bank_mask:0xf
	v_max_f32_e32 v23, v23, v23
	v_max_f32_e32 v8, v8, v23
	v_mov_b32_e32 v23, v201
	s_nop 1
	v_mov_b32_dpp v23, v8 row_ror:8 row_mask:0xf bank_mask:0xf
	v_max_f32_e32 v23, v23, v23
	v_max_f32_e32 v8, v8, v23
	v_mov_b32_e32 v23, v8
	s_nop 1
	v_permlane16_swap_b32_e32 v8, v23
	v_max_f32_e32 v23, v23, v23
	v_max_f32_e32 v8, v8, v8
	v_max_f32_e32 v8, v8, v23
	v_mov_b32_e32 v23, v8
	s_nop 1
	v_permlane32_swap_b32_e32 v8, v23
	v_max_f32_e32 v23, v23, v23
	v_max_f32_e32 v8, v8, v8
	v_max_f32_e32 v8, v8, v23
	v_div_scale_f32 v23, s[20:21], v8, v8, s0
	v_rcp_f32_e32 v32, v23
	v_cmp_lt_f32_e64 s[6:7], 0, v8
	v_fma_f32 v33, -v23, v32, 1.0
	v_fmac_f32_e32 v32, v33, v32
	v_div_scale_f32 v33, vcc, s0, v8, s0
	v_mul_f32_e32 v34, v33, v32
	v_fma_f32 v35, -v23, v34, v33
	v_fmac_f32_e32 v34, v35, v32
	v_fma_f32 v23, -v23, v34, v33
	v_div_fmas_f32 v23, v23, v32, v34
	v_div_fixup_f32 v23, v23, v8, s0
	v_cndmask_b32_e64 v23, 0, v23, s[6:7]
	v_mul_f32_e32 v31, v31, v23
	v_mul_f32_e32 v9, v9, v23
	v_rndne_f32_e32 v31, v31
	v_rndne_f32_e32 v9, v9
	v_cvt_i32_f32_e32 v31, v31
	v_cvt_i32_f32_e32 v9, v9
	global_store_byte v[6:7], v31, off
	global_store_byte v[6:7], v9, off offset:16
	s_and_saveexec_b64 s[6:7], s[4:5]
	s_cbranch_execz .Lcomb_ta
	v_mul_f32_e32 v8, 0x3c010204, v8
	global_store_dword v201, v8, s[14:15]
.Lcomb_ta:
	s_or_b64 exec, exec, s[6:7]
	v_readlane_b32 s0, v255, 0
	v_readlane_b32 s1, v255, 1
	s_add_u32 s14, s14, s0
	s_addc_u32 s15, s15, s1
	v_readlane_b32 s0, v255, 12
	v_readlane_b32 s1, v255, 13
	s_andn2_b64 vcc, exec, s[16:17]
	s_nop 0
	v_lshl_add_u64 v[6:7], v[6:7], 0, s[0:1]
	s_cbranch_vccz .LBB0_2056
	s_waitcnt vmcnt(25)
	v_mov_b64_e32 v[108:109], v[110:111]
	v_lshrrev_b32_e32 v110, 5, v130
	v_and_b32_e32 v110, 0x7fffffc, v110
	global_load_dword v133, v110, s[2:3]
	v_lshrrev_b32_e32 v111, 5, v129
	v_and_b32_e32 v111, 0x7fffffc, v111
	global_load_dword v134, v111, s[2:3]
	global_load_dword v135, v110, s[12:13]
	global_load_dword v123, v111, s[12:13]
	v_readlane_b32 s0, v255, 20
	s_mov_b32 s6, s18
	s_add_i32 s18, s18, s0
	s_cmpk_gt_i32 s18, 0x3fff
	s_cselect_b64 s[16:17], -1, 0
	s_add_i32 s22, s18, s0
	s_cmpk_lt_i32 s22, 0x4000
	s_cselect_b32 s6, s22, s6
	s_ashr_i32 s7, s6, 31
	s_lshl_b64 s[20:21], s[6:7], 8
	v_lshl_add_u64 v[110:111], v[0:1], 0, s[20:21]
	s_mov_b32 s0, 0x400000
	v_mov_b32_e32 v131, v114
	v_add_co_u32_e32 v114, vcc, s0, v110
	v_bfe_i32 v137, v115, 0, 16
	v_ashrrev_i32_e32 v138, 16, v115
	v_addc_co_u32_e32 v115, vcc, 0, v111, vcc
	s_mov_b32 s0, 0x800000
	v_bfe_i32 v139, v116, 0, 16
	v_ashrrev_i32_e32 v140, 16, v116
	v_add_co_u32_e32 v116, vcc, s0, v110
	v_bfe_i32 v141, v117, 0, 16
	v_ashrrev_i32_e32 v142, 16, v117
	v_addc_co_u32_e32 v117, vcc, 0, v111, vcc
	s_mov_b32 s0, 0xc00000
	v_mov_b32_e32 v132, v112
	v_bfe_i32 v130, v113, 0, 16
	v_ashrrev_i32_e32 v136, 16, v113
	global_load_dword v112, v[110:111], off
	global_load_dword v113, v[116:117], off
	v_add_co_u32_e32 v116, vcc, s0, v110
	global_load_dword v114, v[114:115], off
	s_nop 0
	v_addc_co_u32_e32 v117, vcc, 0, v111, vcc
	s_mov_b32 s0, 0x1000000
	global_load_dword v115, v[116:117], off
	v_add_co_u32_e32 v116, vcc, s0, v110
	s_mov_b32 s0, 0x1400000
	s_nop 0
	v_addc_co_u32_e32 v117, vcc, 0, v111, vcc
	v_bfe_i32 v143, v118, 0, 16
	v_ashrrev_i32_e32 v144, 16, v118
	v_add_co_u32_e32 v118, vcc, s0, v110
	v_bfe_i32 v145, v119, 0, 16
	v_ashrrev_i32_e32 v146, 16, v119
	v_addc_co_u32_e32 v119, vcc, 0, v111, vcc
	s_mov_b32 s0, 0x1800000
	global_load_dword v116, v[116:117], off
	v_bfe_i32 v147, v120, 0, 16
	global_load_dword v117, v[118:119], off
	v_add_co_u32_e32 v118, vcc, s0, v110
	s_mov_b32 s0, 0x1c00000
	s_nop 0
	v_addc_co_u32_e32 v119, vcc, 0, v111, vcc
	v_ashrrev_i32_e32 v148, 16, v120
	v_add_co_u32_e32 v120, vcc, s0, v110
	v_bfe_i32 v149, v121, 0, 16
	v_ashrrev_i32_e32 v150, 16, v121
	v_addc_co_u32_e32 v121, vcc, 0, v111, vcc
	s_brev_b32 s0, 64
	global_load_dword v118, v[118:119], off
	v_bfe_i32 v153, v124, 0, 16
	global_load_dword v119, v[120:121], off
	v_add_co_u32_e32 v120, vcc, s0, v110
	s_mov_b32 s0, 0x2400000
	s_nop 0
	v_addc_co_u32_e32 v121, vcc, 0, v111, vcc
	v_ashrrev_i32_e32 v154, 16, v124
	v_add_co_u32_e32 v124, vcc, s0, v110
	v_bfe_i32 v155, v125, 0, 16
	v_ashrrev_i32_e32 v156, 16, v125
	v_addc_co_u32_e32 v125, vcc, 0, v111, vcc
	s_mov_b32 s0, 0x2800000
	global_load_dword v120, v[120:121], off
	v_bfe_i32 v151, v122, 0, 16
	global_load_dword v121, v[124:125], off
	v_add_co_u32_e32 v124, vcc, s0, v110
	s_mov_b32 s0, 0x2c00000
	s_nop 0
	v_addc_co_u32_e32 v125, vcc, 0, v111, vcc
	v_ashrrev_i32_e32 v152, 16, v122
	global_load_dword v122, v[124:125], off
	v_add_co_u32_e32 v124, vcc, s0, v110
	s_mov_b32 s0, 0x3000000
	s_nop 0
	v_addc_co_u32_e32 v125, vcc, 0, v111, vcc
	v_bfe_i32 v157, v126, 0, 16
	v_ashrrev_i32_e32 v158, 16, v126
	v_add_co_u32_e32 v126, vcc, s0, v110
	v_bfe_i32 v159, v127, 0, 16
	v_ashrrev_i32_e32 v160, 16, v127
	v_addc_co_u32_e32 v127, vcc, 0, v111, vcc
	s_mov_b32 s0, 0x3400000
	global_load_dword v124, v[124:125], off
	v_bfe_i32 v161, v128, 0, 16
	global_load_dword v125, v[126:127], off
	v_add_co_u32_e32 v126, vcc, s0, v110
	s_mov_b32 s0, 0x3800000
	s_nop 0
	v_addc_co_u32_e32 v127, vcc, 0, v111, vcc
	v_ashrrev_i32_e32 v162, 16, v128
	v_add_co_u32_e32 v128, vcc, s0, v110
	s_mov_b32 s0, 0x3c00000
	s_nop 0
	v_addc_co_u32_e32 v129, vcc, 0, v111, vcc
	v_add_co_u32_e32 v110, vcc, s0, v110
	global_load_dword v126, v[126:127], off
	s_nop 0
	v_addc_co_u32_e32 v111, vcc, 0, v111, vcc
	global_load_dword v127, v[128:129], off
	s_lshl_b64 s[6:7], s[6:7], 9
	global_load_dword v128, v[110:111], off
	v_add_u32_sdwa v110, sext(v131), sext(v132) dst_sel:DWORD dst_unused:UNUSED_PAD src0_sel:WORD_0 src1_sel:WORD_0
	v_add3_u32 v110, v110, v130, v137
	v_add3_u32 v110, v110, v139, v141
	v_add3_u32 v110, v110, v143, v145
	v_add3_u32 v110, v110, v147, v149
	v_add_u32_sdwa v111, sext(v131), sext(v132) dst_sel:DWORD dst_unused:UNUSED_PAD src0_sel:WORD_1 src1_sel:WORD_1
	v_add3_u32 v110, v110, v151, v153
	v_add3_u32 v111, v111, v136, v138
	v_add3_u32 v110, v110, v155, v157
	v_add3_u32 v111, v111, v140, v142
	v_add3_u32 v131, v110, v159, v161
	v_add3_u32 v111, v111, v144, v146
	v_cvt_f32_i32_e32 v131, v131
	v_add3_u32 v111, v111, v148, v150
	v_add3_u32 v111, v111, v152, v154
	v_add3_u32 v111, v111, v156, v158
	s_waitcnt vmcnt(19)
	v_mul_f32_e32 v133, 0x40810204, v133
	v_add3_u32 v132, v111, v160, v162
	v_lshl_add_u64 v[110:111], v[4:5], 0, s[6:7]
	v_mul_f32_e32 v131, v133, v131
	global_load_dword v130, v[110:111], off
	global_load_dword v129, v[110:111], off offset:64
	v_lshl_add_u64 v[110:111], v[2:3], 0, s[6:7]
	v_mul_f32_e32 v133, 0x3d372713, v131
	global_load_dwordx2 v[110:111], v[110:111], off
	v_mul_f32_e32 v133, v131, v133
	v_fma_f32 v133, v131, v133, v131
	v_mul_f32_e32 v133, 0x3f4c422a, v133
	v_add_f32_e32 v133, v133, v133
	v_mul_f32_e32 v133, 0xbfb8aa3b, v133
	v_exp_f32_e32 v133, v133
	s_waitcnt vmcnt(21)
	v_mul_f32_e32 v134, 0x40810204, v134
	s_mov_b32 s0, 0x42fe0000
	v_readlane_b32 s1, v255, 21
	v_add_f32_e32 v133, 1.0, v133
	v_rcp_f32_e32 v133, v133
	s_nop 0
	v_mul_f32_e32 v131, v131, v133
	v_mul_f32_e32 v108, v108, v131
	s_waitcnt vmcnt(20)
	v_mul_f32_e32 v131, v135, v108
	v_cvt_f32_i32_e32 v108, v132
	v_mul_f32_e32 v108, v134, v108
	v_mul_f32_e32 v132, 0x3d372713, v108
	v_mul_f32_e32 v132, v108, v132
	v_fma_f32 v132, v108, v132, v108
	v_mul_f32_e32 v132, 0x3f4c422a, v132
	v_add_f32_e32 v132, v132, v132
	v_mul_f32_e32 v132, 0xbfb8aa3b, v132
	v_exp_f32_e32 v132, v132
	s_nop 0
	v_add_f32_e32 v132, 1.0, v132
	v_rcp_f32_e32 v132, v132
	s_nop 0
	v_mul_f32_e32 v108, v108, v132
	v_mul_f32_e32 v108, v109, v108
	s_waitcnt vmcnt(19)
	v_mul_f32_e32 v109, v123, v108
	v_max_f32_e64 v108, |v131|, |v109|
	v_mov_b32_e32 v123, v201
	s_nop 1
	v_mov_b32_dpp v123, v108 row_ror:1 row_mask:0xf bank_mask:0xf
	v_max_f32_e32 v123, v123, v123
	v_max_f32_e32 v108, v108, v123
	v_mov_b32_e32 v123, v201
	s_nop 1
	v_mov_b32_dpp v123, v108 row_ror:2 row_mask:0xf bank_mask:0xf
	v_max_f32_e32 v123, v123, v123
	v_max_f32_e32 v108, v108, v123
	v_mov_b32_e32 v123, v201
	s_nop 1
	v_mov_b32_dpp v123, v108 row_ror:4 row_mask:0xf bank_mask:0xf
	v_max_f32_e32 v123, v123, v123
	v_max_f32_e32 v108, v108, v123
	v_mov_b32_e32 v123, v201
	s_nop 1
	v_mov_b32_dpp v123, v108 row_ror:8 row_mask:0xf bank_mask:0xf
	v_max_f32_e32 v123, v123, v123
	v_max_f32_e32 v108, v108, v123
	v_mov_b32_e32 v123, v108
	s_nop 1
	v_permlane16_swap_b32_e32 v108, v123
	v_max_f32_e32 v123, v123, v123
	v_max_f32_e32 v108, v108, v108
	v_max_f32_e32 v108, v108, v123
	v_mov_b32_e32 v123, v108
	s_nop 1
	v_permlane32_swap_b32_e32 v108, v123
	v_max_f32_e32 v123, v123, v123
	v_max_f32_e32 v108, v108, v108
	v_max_f32_e32 v108, v108, v123
	v_div_scale_f32 v123, s[20:21], v108, v108, s0
	v_rcp_f32_e32 v132, v123
	v_cmp_lt_f32_e64 s[6:7], 0, v108
	v_fma_f32 v133, -v123, v132, 1.0
	v_fmac_f32_e32 v132, v133, v132
	v_div_scale_f32 v133, vcc, s0, v108, s0
	v_mul_f32_e32 v134, v133, v132
	v_fma_f32 v135, -v123, v134, v133
	v_fmac_f32_e32 v134, v135, v132
	v_fma_f32 v123, -v123, v134, v133
	v_div_fmas_f32 v123, v123, v132, v134
	v_div_fixup_f32 v123, v123, v108, s0
	v_cndmask_b32_e64 v123, 0, v123, s[6:7]
	v_mul_f32_e32 v131, v131, v123
	v_mul_f32_e32 v109, v109, v123
	v_rndne_f32_e32 v131, v131
	v_rndne_f32_e32 v109, v109
	v_cvt_i32_f32_e32 v131, v131
	v_cvt_i32_f32_e32 v109, v109
	global_store_byte v[6:7], v131, off
	global_store_byte v[6:7], v109, off offset:16
	s_and_saveexec_b64 s[6:7], s[4:5]
	s_cbranch_execz .Lcomb_tb
	v_mul_f32_e32 v108, 0x3c010204, v108
	global_store_dword v201, v108, s[14:15]
.Lcomb_tb:
	s_or_b64 exec, exec, s[6:7]
	v_readlane_b32 s0, v255, 0
	v_readlane_b32 s1, v255, 1
	s_add_u32 s14, s14, s0
	s_addc_u32 s15, s15, s1
	v_readlane_b32 s0, v255, 12
	v_readlane_b32 s1, v255, 13
	s_andn2_b64 vcc, exec, s[16:17]
	s_nop 0
	v_lshl_add_u64 v[6:7], v[6:7], 0, s[0:1]
	s_cbranch_vccz .LBB0_2056
	s_waitcnt vmcnt(27)
	s_branch .LBB0_2054
